# speedup vs baseline: 1.0254x; 1.0035x over previous
_Z11prep_kernelPKfPjPfS1_:
	s_load_dwordx4 s[4:7], s[0:1], 0x0
	s_and_b32 s3, s2, 7
	s_lshr_b32 s8, s2, 3
	s_lshr_b32 s9, s3, 1
	s_lshl_b32 s9, s9, 7
	s_and_b32 s3, s3, 1
	s_lshl_b32 s3, s3, 6
	s_add_i32 s2, s9, s8
	s_add_i32 s2, s2, s3
	v_or_b32_e32 v1, s2, v0
	v_cmp_eq_u32_e32 vcc, 0, v1
	s_and_saveexec_b64 s[8:9], vcc
	s_cbranch_execz .LBB0_2
	s_load_dwordx2 s[10:11], s[0:1], 0x18
	v_mov_b32_e32 v1, 0
	s_waitcnt lgkmcnt(0)
	global_store_dword v1, v1, s[10:11]
	global_store_dword v1, v1, s[10:11] offset:-4096
	global_store_dword v1, v1, s[10:11] offset:-4092
	global_store_dword v1, v1, s[10:11] offset:-4088
	global_store_dword v1, v1, s[10:11] offset:-4084
	global_store_dword v1, v1, s[10:11] offset:-4080
	global_store_dword v1, v1, s[10:11] offset:-4076
	global_store_dword v1, v1, s[10:11] offset:-4072
	global_store_dword v1, v1, s[10:11] offset:-4068
	global_store_dword v1, v1, s[10:11] offset:-4064
	global_store_dword v1, v1, s[10:11] offset:-4060
